# phase prologues: combine parameter vectors, MoE unit search and conditioning silu loaded with all loads in flight (were serialized round trips)
# speedup vs baseline: 1.0189x; 1.0106x over previous
; #define LAS __attribute__((address_space(3)))
; __device__ __forceinline__ float silu_f(float x) { return x * __builtin_amdgcn_rcpf(1.0f + __expf(-x)); }
; __device__ __forceinline__ void p0_mod(const Frame& F, const Args& a) {
;     LAS float* sv = (LAS float*)F.lds;
;     LAS float* red = (LAS float*)(F.lds + 32768);
;     for (int i = F.tid; i < 3 * D; i += NTHREADS) { const int r = i / D, k = i % D; const float v = r < 2 ? a.in[I_C][r * D + k] : a.in[I_CCTX][k]; sv[i] = silu_f(v); }
;     __syncthreads();
.LBB0_67:
	v_mov_b32_e32 v3, 0
	s_waitcnt lgkmcnt(0)
	v_lshl_add_u64 v[4:5], s[70:71], 0, v[2:3]
	v_add_u32_e32 v6, 0, v2
	s_mov_b64 s[0:1], 0
	s_movk_i32 s2, 0x1000
	s_mov_b64 s[4:5], 0x800
	s_movk_i32 s6, 0x15ff
	v_mov_b32_e32 v7, v0
	s_barrier
	global_load_dword v10, v2, s[70:71]
	s_add_u32 s4, s70, 0x800
	s_addc_u32 s5, s71, 0
	global_load_dword v11, v2, s[4:5]
	s_add_u32 s4, s70, 0x1000
	s_addc_u32 s5, s71, 0
	global_load_dword v12, v2, s[4:5]
	s_add_u32 s4, s70, 0x1800
	s_addc_u32 s5, s71, 0
	global_load_dword v13, v2, s[4:5]
	s_add_u32 s4, s70, 0x2000
	s_addc_u32 s5, s71, 0
	global_load_dword v14, v2, s[4:5]
	s_add_u32 s4, s70, 0x2800
	s_addc_u32 s5, s71, 0
	global_load_dword v15, v2, s[4:5]
	s_add_u32 s4, s70, 0x3000
	s_addc_u32 s5, s71, 0
	global_load_dword v16, v2, s[4:5]
	s_add_u32 s4, s70, 0x3800
	s_addc_u32 s5, s71, 0
	global_load_dword v17, v2, s[4:5]
	global_load_dword v18, v2, s[74:75]
	s_add_u32 s4, s74, 0x800
	s_addc_u32 s5, s75, 0
	global_load_dword v19, v2, s[4:5]
	s_add_u32 s4, s74, 0x1000
	s_addc_u32 s5, s75, 0
	global_load_dword v20, v2, s[4:5]
	s_add_u32 s4, s74, 0x1800
	s_addc_u32 s5, s75, 0
	global_load_dword v21, v2, s[4:5]
	s_waitcnt vmcnt(0)
	v_mul_f32_e32 v9, 0xbfb8aa3b, v10
	v_exp_f32_e32 v9, v9
	s_nop 0
	v_add_f32_e32 v7, 1.0, v9
	v_rcp_f32_e32 v9, v7
	s_nop 0
	v_mul_f32_e32 v8, v10, v9
	ds_write_b32 v6, v8
	v_mul_f32_e32 v9, 0xbfb8aa3b, v11
	v_exp_f32_e32 v9, v9
	s_nop 0
	v_add_f32_e32 v7, 1.0, v9
	v_rcp_f32_e32 v9, v7
	s_nop 0
	v_mul_f32_e32 v8, v11, v9
	ds_write_b32 v6, v8 offset:2048
	v_mul_f32_e32 v9, 0xbfb8aa3b, v12
	v_exp_f32_e32 v9, v9
	s_nop 0
	v_add_f32_e32 v7, 1.0, v9
	v_rcp_f32_e32 v9, v7
	s_nop 0
	v_mul_f32_e32 v8, v12, v9
	ds_write_b32 v6, v8 offset:4096
	v_mul_f32_e32 v9, 0xbfb8aa3b, v13
	v_exp_f32_e32 v9, v9
	s_nop 0
	v_add_f32_e32 v7, 1.0, v9
	v_rcp_f32_e32 v9, v7
	s_nop 0
	v_mul_f32_e32 v8, v13, v9
	ds_write_b32 v6, v8 offset:6144
	v_mul_f32_e32 v9, 0xbfb8aa3b, v14
	v_exp_f32_e32 v9, v9
	s_nop 0
	v_add_f32_e32 v7, 1.0, v9
	v_rcp_f32_e32 v9, v7
	s_nop 0
	v_mul_f32_e32 v8, v14, v9
	ds_write_b32 v6, v8 offset:8192
	v_mul_f32_e32 v9, 0xbfb8aa3b, v15
	v_exp_f32_e32 v9, v9
	s_nop 0
	v_add_f32_e32 v7, 1.0, v9
	v_rcp_f32_e32 v9, v7
	s_nop 0
	v_mul_f32_e32 v8, v15, v9
	ds_write_b32 v6, v8 offset:10240
	v_mul_f32_e32 v9, 0xbfb8aa3b, v16
	v_exp_f32_e32 v9, v9
	s_nop 0
	v_add_f32_e32 v7, 1.0, v9
	v_rcp_f32_e32 v9, v7
	s_nop 0
	v_mul_f32_e32 v8, v16, v9
	ds_write_b32 v6, v8 offset:12288
	v_mul_f32_e32 v9, 0xbfb8aa3b, v17
	v_exp_f32_e32 v9, v9
	s_nop 0
	v_add_f32_e32 v7, 1.0, v9
	v_rcp_f32_e32 v9, v7
	s_nop 0
	v_mul_f32_e32 v8, v17, v9
	ds_write_b32 v6, v8 offset:14336
	v_mul_f32_e32 v9, 0xbfb8aa3b, v18
	v_exp_f32_e32 v9, v9
	s_nop 0
	v_add_f32_e32 v7, 1.0, v9
	v_rcp_f32_e32 v9, v7
	s_nop 0
	v_mul_f32_e32 v8, v18, v9
	ds_write_b32 v6, v8 offset:16384
	v_mul_f32_e32 v9, 0xbfb8aa3b, v19
	v_exp_f32_e32 v9, v9
	s_nop 0
	v_add_f32_e32 v7, 1.0, v9
	v_rcp_f32_e32 v9, v7
	s_nop 0
	v_mul_f32_e32 v8, v19, v9
	ds_write_b32 v6, v8 offset:18432
	v_mul_f32_e32 v9, 0xbfb8aa3b, v20
	v_exp_f32_e32 v9, v9
	s_nop 0
	v_add_f32_e32 v7, 1.0, v9
	v_rcp_f32_e32 v9, v7
	s_nop 0
	v_mul_f32_e32 v8, v20, v9
	ds_write_b32 v6, v8 offset:20480
	v_mul_f32_e32 v9, 0xbfb8aa3b, v21
	v_exp_f32_e32 v9, v9
	s_nop 0
	v_add_f32_e32 v7, 1.0, v9
	v_rcp_f32_e32 v9, v7
	s_nop 0
	v_mul_f32_e32 v8, v21, v9
	ds_write_b32 v6, v8 offset:22528
	s_or_b64 exec, exec, s[0:1]
	s_cmpk_gt_i32 s3, 0xff
	s_waitcnt lgkmcnt(0)
	s_barrier
	s_cbranch_scc1 .LBB0_101
	v_mul_lo_u16_e32 v2, 43, v1
	v_lshrrev_b16_e32 v8, 10, v2
	v_mul_u32_u24_e32 v4, 0x2ab, v0
	v_mul_lo_u16_e32 v2, 24, v8
	v_lshrrev_b32_e32 v4, 16, v4
	s_add_u32 s0, s92, 0x100000
	v_sub_u16_e32 v2, v1, v2
	v_add_u32_e32 v3, 24, v0
	v_readlane_b32 s12, v254, 44
	s_movk_i32 s2, 0x120
	v_mul_lo_u16_e32 v6, 0x60, v4
	v_mbcnt_lo_u32_b32 v7, -1, 0
	s_addc_u32 s1, s93, 0
	v_and_b32_e32 v2, 0xff, v2
	v_and_b32_e32 v5, 63, v3
	v_cmp_gt_u32_e64 s[6:7], s2, v0
	v_sub_u16_e32 v6, v0, v6
	v_mbcnt_hi_u32_b32 v7, -1, v7
	s_lshl_b32 s2, s12, 10
	v_lshl_add_u32 v9, v2, 4, 0
	s_mul_i32 s10, s12, 0x480
	v_lshlrev_b32_e32 v2, 2, v2
	v_lshl_add_u32 v10, v6, 2, 0
	v_mul_u32_u24_e32 v11, 0x180, v4
	v_and_or_b32 v5, v7, 64, v5
	s_add_i32 s2, s2, 0
	v_cmp_gt_u32_e32 vcc, 48, v1
	v_cmp_gt_u32_e64 s[4:5], 24, v1
	s_mov_b32 s11, 0
	v_mov_b32_e32 v3, 0
	v_lshlrev_b32_e32 v5, 2, v5
	v_lshl_or_b32 v7, s12, 8, v8
	v_lshl_add_u32 v24, v8, 2, s2
	v_lshlrev_b32_e32 v2, 2, v2
	s_mov_b32 s2, 0xc000
	v_add_u32_e32 v25, v10, v11
	v_lshlrev_b32_e32 v8, 2, v6
	v_add_u32_e32 v26, s10, v9
	s_mov_b32 s14, s3
	s_branch .LBB0_72

;     ...
;     __syncthreads();
;     if (F.tid < 32) { const int geff = tb[200], c = tb[201]; const int L = F.tid * geff + c; i32x4 v = {0, 0, 0, 0};
;         if (!tb[202] && L < tb[65]) { int e = 0; while (L >= tb[e + 1]) ++e;
;             const int rem = L - tb[e], t = tb[66 + e], mt = rem % t, nt = rem / t; v = (i32x4){e, tb[132 + e] + mt * 256, nt, 1}; }
;         ut[F.tid] = v; }
.LBB0_1595:
	s_or_b64 exec, exec, s[4:5]
	v_cmp_gt_u32_e32 vcc, 32, v0
	s_waitcnt vmcnt(0) lgkmcnt(0)
	s_barrier
	s_and_saveexec_b64 s[4:5], vcc
	s_cbranch_execz .LBB0_1603
	s_add_i32 s2, 0, 0x23b20
	v_mov_b32_e32 v2, s2
	ds_read_b96 v[6:8], v2
	v_mov_b32_e32 v2, 0
	v_mov_b32_e32 v3, 0
	v_mov_b32_e32 v4, 0
	v_mov_b32_e32 v5, 0
	s_waitcnt lgkmcnt(0)
	v_cmp_ne_u32_e32 vcc, 0, v8
	s_cbranch_vccnz .LBB0_1602
	s_add_i32 s2, 0, 0x23904
	v_mov_b32_e32 v2, s2
	ds_read_b32 v2, v2
	v_mul_lo_u32 v3, v6, v0
	v_add_u32_e32 v6, v3, v7
	v_mov_b32_e32 v5, 0
	v_mov_b32_e32 v4, 0
	s_waitcnt lgkmcnt(0)
	v_cmp_lt_i32_e32 vcc, v6, v2
	v_mov_b32_e32 v3, 0
	v_mov_b32_e32 v2, 0
	s_and_saveexec_b64 s[6:7], vcc
	s_cbranch_execz .LBB0_1601
	v_mov_b32_e32 v2, 0
	v_mov_b32_e32 v3, 0x23804
	ds_read_b32 v10, v3 offset:0
	ds_read_b32 v11, v3 offset:4
	ds_read_b32 v12, v3 offset:8
	ds_read_b32 v13, v3 offset:12
	ds_read_b32 v14, v3 offset:16
	ds_read_b32 v15, v3 offset:20
	ds_read_b32 v16, v3 offset:24
	ds_read_b32 v17, v3 offset:28
	ds_read_b32 v18, v3 offset:32
	ds_read_b32 v19, v3 offset:36
	ds_read_b32 v20, v3 offset:40
	ds_read_b32 v21, v3 offset:44
	ds_read_b32 v22, v3 offset:48
	ds_read_b32 v23, v3 offset:52
	ds_read_b32 v24, v3 offset:56
	ds_read_b32 v25, v3 offset:60
	s_waitcnt lgkmcnt(0)
	v_cmp_le_i32_e32 vcc, v10, v6
	s_nop 1
	v_addc_co_u32_e32 v2, vcc, 0, v2, vcc
	v_cmp_le_i32_e32 vcc, v11, v6
	s_nop 1
	v_addc_co_u32_e32 v2, vcc, 0, v2, vcc
	v_cmp_le_i32_e32 vcc, v12, v6
	s_nop 1
	v_addc_co_u32_e32 v2, vcc, 0, v2, vcc
	v_cmp_le_i32_e32 vcc, v13, v6
	s_nop 1
	v_addc_co_u32_e32 v2, vcc, 0, v2, vcc
	v_cmp_le_i32_e32 vcc, v14, v6
	s_nop 1
	v_addc_co_u32_e32 v2, vcc, 0, v2, vcc
	v_cmp_le_i32_e32 vcc, v15, v6
	s_nop 1
	v_addc_co_u32_e32 v2, vcc, 0, v2, vcc
	v_cmp_le_i32_e32 vcc, v16, v6
	s_nop 1
	v_addc_co_u32_e32 v2, vcc, 0, v2, vcc
	v_cmp_le_i32_e32 vcc, v17, v6
	s_nop 1
	v_addc_co_u32_e32 v2, vcc, 0, v2, vcc
	v_cmp_le_i32_e32 vcc, v18, v6
	s_nop 1
	v_addc_co_u32_e32 v2, vcc, 0, v2, vcc
	v_cmp_le_i32_e32 vcc, v19, v6
	s_nop 1
	v_addc_co_u32_e32 v2, vcc, 0, v2, vcc
	v_cmp_le_i32_e32 vcc, v20, v6
	s_nop 1
	v_addc_co_u32_e32 v2, vcc, 0, v2, vcc
	v_cmp_le_i32_e32 vcc, v21, v6
	s_nop 1
	v_addc_co_u32_e32 v2, vcc, 0, v2, vcc
	v_cmp_le_i32_e32 vcc, v22, v6
	s_nop 1
	v_addc_co_u32_e32 v2, vcc, 0, v2, vcc
	v_cmp_le_i32_e32 vcc, v23, v6
	s_nop 1
	v_addc_co_u32_e32 v2, vcc, 0, v2, vcc
	v_cmp_le_i32_e32 vcc, v24, v6
	s_nop 1
	v_addc_co_u32_e32 v2, vcc, 0, v2, vcc
	v_cmp_le_i32_e32 vcc, v25, v6
	s_nop 1
	v_addc_co_u32_e32 v2, vcc, 0, v2, vcc
	ds_read_b32 v10, v3 offset:64
	ds_read_b32 v11, v3 offset:68
	ds_read_b32 v12, v3 offset:72
	ds_read_b32 v13, v3 offset:76
	ds_read_b32 v14, v3 offset:80
	ds_read_b32 v15, v3 offset:84
	ds_read_b32 v16, v3 offset:88
	ds_read_b32 v17, v3 offset:92
	ds_read_b32 v18, v3 offset:96
	ds_read_b32 v19, v3 offset:100
	ds_read_b32 v20, v3 offset:104
	ds_read_b32 v21, v3 offset:108
	ds_read_b32 v22, v3 offset:112
	ds_read_b32 v23, v3 offset:116
	ds_read_b32 v24, v3 offset:120
	ds_read_b32 v25, v3 offset:124
	s_waitcnt lgkmcnt(0)
	v_cmp_le_i32_e32 vcc, v10, v6
	s_nop 1
	v_addc_co_u32_e32 v2, vcc, 0, v2, vcc
	v_cmp_le_i32_e32 vcc, v11, v6
	s_nop 1
	v_addc_co_u32_e32 v2, vcc, 0, v2, vcc
	v_cmp_le_i32_e32 vcc, v12, v6
	s_nop 1
	v_addc_co_u32_e32 v2, vcc, 0, v2, vcc
	v_cmp_le_i32_e32 vcc, v13, v6
	s_nop 1
	v_addc_co_u32_e32 v2, vcc, 0, v2, vcc
	v_cmp_le_i32_e32 vcc, v14, v6
	s_nop 1
	v_addc_co_u32_e32 v2, vcc, 0, v2, vcc
	v_cmp_le_i32_e32 vcc, v15, v6
	s_nop 1
	v_addc_co_u32_e32 v2, vcc, 0, v2, vcc
	v_cmp_le_i32_e32 vcc, v16, v6
	s_nop 1
	v_addc_co_u32_e32 v2, vcc, 0, v2, vcc
	v_cmp_le_i32_e32 vcc, v17, v6
	s_nop 1
	v_addc_co_u32_e32 v2, vcc, 0, v2, vcc
	v_cmp_le_i32_e32 vcc, v18, v6
	s_nop 1
	v_addc_co_u32_e32 v2, vcc, 0, v2, vcc
	v_cmp_le_i32_e32 vcc, v19, v6
	s_nop 1
	v_addc_co_u32_e32 v2, vcc, 0, v2, vcc
	v_cmp_le_i32_e32 vcc, v20, v6
	s_nop 1
	v_addc_co_u32_e32 v2, vcc, 0, v2, vcc
	v_cmp_le_i32_e32 vcc, v21, v6
	s_nop 1
	v_addc_co_u32_e32 v2, vcc, 0, v2, vcc
	v_cmp_le_i32_e32 vcc, v22, v6
	s_nop 1
	v_addc_co_u32_e32 v2, vcc, 0, v2, vcc
	v_cmp_le_i32_e32 vcc, v23, v6
	s_nop 1
	v_addc_co_u32_e32 v2, vcc, 0, v2, vcc
	v_cmp_le_i32_e32 vcc, v24, v6
	s_nop 1
	v_addc_co_u32_e32 v2, vcc, 0, v2, vcc
	v_cmp_le_i32_e32 vcc, v25, v6
	s_nop 1
	v_addc_co_u32_e32 v2, vcc, 0, v2, vcc
	ds_read_b32 v10, v3 offset:128
	ds_read_b32 v11, v3 offset:132
	ds_read_b32 v12, v3 offset:136
	ds_read_b32 v13, v3 offset:140
	ds_read_b32 v14, v3 offset:144
	ds_read_b32 v15, v3 offset:148
	ds_read_b32 v16, v3 offset:152
	ds_read_b32 v17, v3 offset:156
	ds_read_b32 v18, v3 offset:160
	ds_read_b32 v19, v3 offset:164
	ds_read_b32 v20, v3 offset:168
	ds_read_b32 v21, v3 offset:172
	ds_read_b32 v22, v3 offset:176
	ds_read_b32 v23, v3 offset:180
	ds_read_b32 v24, v3 offset:184
	ds_read_b32 v25, v3 offset:188
	s_waitcnt lgkmcnt(0)
;     ...
;     if (F.tid < 32) { const int geff = tb[200], c = tb[201]; const int L = F.tid * geff + c; i32x4 v = {0, 0, 0, 0};
;         if (!tb[202] && L < tb[65]) { int e = 0; while (L >= tb[e + 1]) ++e;
;             const int rem = L - tb[e], t = tb[66 + e], mt = rem % t, nt = rem / t; v = (i32x4){e, tb[132 + e] + mt * 256, nt, 1}; }
;         ut[F.tid] = v; }
	v_cmp_le_i32_e32 vcc, v10, v6
	s_nop 1
	v_addc_co_u32_e32 v2, vcc, 0, v2, vcc
	v_cmp_le_i32_e32 vcc, v11, v6
	s_nop 1
	v_addc_co_u32_e32 v2, vcc, 0, v2, vcc
	v_cmp_le_i32_e32 vcc, v12, v6
	s_nop 1
	v_addc_co_u32_e32 v2, vcc, 0, v2, vcc
	v_cmp_le_i32_e32 vcc, v13, v6
	s_nop 1
	v_addc_co_u32_e32 v2, vcc, 0, v2, vcc
	v_cmp_le_i32_e32 vcc, v14, v6
	s_nop 1
	v_addc_co_u32_e32 v2, vcc, 0, v2, vcc
	v_cmp_le_i32_e32 vcc, v15, v6
	s_nop 1
	v_addc_co_u32_e32 v2, vcc, 0, v2, vcc
	v_cmp_le_i32_e32 vcc, v16, v6
	s_nop 1
	v_addc_co_u32_e32 v2, vcc, 0, v2, vcc
	v_cmp_le_i32_e32 vcc, v17, v6
	s_nop 1
	v_addc_co_u32_e32 v2, vcc, 0, v2, vcc
	v_cmp_le_i32_e32 vcc, v18, v6
	s_nop 1
	v_addc_co_u32_e32 v2, vcc, 0, v2, vcc
	v_cmp_le_i32_e32 vcc, v19, v6
	s_nop 1
	v_addc_co_u32_e32 v2, vcc, 0, v2, vcc
	v_cmp_le_i32_e32 vcc, v20, v6
	s_nop 1
	v_addc_co_u32_e32 v2, vcc, 0, v2, vcc
	v_cmp_le_i32_e32 vcc, v21, v6
	s_nop 1
	v_addc_co_u32_e32 v2, vcc, 0, v2, vcc
	v_cmp_le_i32_e32 vcc, v22, v6
	s_nop 1
	v_addc_co_u32_e32 v2, vcc, 0, v2, vcc
	v_cmp_le_i32_e32 vcc, v23, v6
	s_nop 1
	v_addc_co_u32_e32 v2, vcc, 0, v2, vcc
	v_cmp_le_i32_e32 vcc, v24, v6
	s_nop 1
	v_addc_co_u32_e32 v2, vcc, 0, v2, vcc
	v_cmp_le_i32_e32 vcc, v25, v6
	s_nop 1
	v_addc_co_u32_e32 v2, vcc, 0, v2, vcc
	ds_read_b32 v10, v3 offset:192
	ds_read_b32 v11, v3 offset:196
	ds_read_b32 v12, v3 offset:200
	ds_read_b32 v13, v3 offset:204
	ds_read_b32 v14, v3 offset:208
	ds_read_b32 v15, v3 offset:212
	ds_read_b32 v16, v3 offset:216
	ds_read_b32 v17, v3 offset:220
	ds_read_b32 v18, v3 offset:224
	ds_read_b32 v19, v3 offset:228
	ds_read_b32 v20, v3 offset:232
	ds_read_b32 v21, v3 offset:236
	ds_read_b32 v22, v3 offset:240
	ds_read_b32 v23, v3 offset:244
	ds_read_b32 v24, v3 offset:248
	ds_read_b32 v25, v3 offset:252
	s_waitcnt lgkmcnt(0)
	v_cmp_le_i32_e32 vcc, v10, v6
	s_nop 1
	v_addc_co_u32_e32 v2, vcc, 0, v2, vcc
	v_cmp_le_i32_e32 vcc, v11, v6
	s_nop 1
	v_addc_co_u32_e32 v2, vcc, 0, v2, vcc
	v_cmp_le_i32_e32 vcc, v12, v6
	s_nop 1
	v_addc_co_u32_e32 v2, vcc, 0, v2, vcc
	v_cmp_le_i32_e32 vcc, v13, v6
	s_nop 1
	v_addc_co_u32_e32 v2, vcc, 0, v2, vcc
	v_cmp_le_i32_e32 vcc, v14, v6
	s_nop 1
	v_addc_co_u32_e32 v2, vcc, 0, v2, vcc
	v_cmp_le_i32_e32 vcc, v15, v6
	s_nop 1
	v_addc_co_u32_e32 v2, vcc, 0, v2, vcc
	v_cmp_le_i32_e32 vcc, v16, v6
	s_nop 1
	v_addc_co_u32_e32 v2, vcc, 0, v2, vcc
	v_cmp_le_i32_e32 vcc, v17, v6
	s_nop 1
	v_addc_co_u32_e32 v2, vcc, 0, v2, vcc
	v_cmp_le_i32_e32 vcc, v18, v6
	s_nop 1
	v_addc_co_u32_e32 v2, vcc, 0, v2, vcc
	v_cmp_le_i32_e32 vcc, v19, v6
	s_nop 1
	v_addc_co_u32_e32 v2, vcc, 0, v2, vcc
	v_cmp_le_i32_e32 vcc, v20, v6
	s_nop 1
	v_addc_co_u32_e32 v2, vcc, 0, v2, vcc
	v_cmp_le_i32_e32 vcc, v21, v6
	s_nop 1
	v_addc_co_u32_e32 v2, vcc, 0, v2, vcc
	v_cmp_le_i32_e32 vcc, v22, v6
	s_nop 1
	v_addc_co_u32_e32 v2, vcc, 0, v2, vcc
	v_cmp_le_i32_e32 vcc, v23, v6
	s_nop 1
	v_addc_co_u32_e32 v2, vcc, 0, v2, vcc
	v_cmp_le_i32_e32 vcc, v24, v6
	s_nop 1
	v_addc_co_u32_e32 v2, vcc, 0, v2, vcc
	v_cmp_le_i32_e32 vcc, v25, v6
	s_nop 1
	v_addc_co_u32_e32 v2, vcc, 0, v2, vcc
	v_lshl_add_u32 v3, v2, 2, 0
	v_add_u32_e32 v3, 0x23800, v3
	ds_read2_b32 v[8:9], v3 offset1:66
	ds_read_b32 v3, v3 offset:528
	v_mov_b32_e32 v5, 1
	s_waitcnt lgkmcnt(1)
	v_sub_u32_e32 v4, 0, v9
	v_max_i32_e32 v4, v9, v4
	v_cvt_f32_u32_e32 v7, v4
	v_sub_u32_e32 v11, 0, v4
	v_sub_u32_e32 v6, v6, v8
	v_sub_u32_e32 v10, 0, v6
	v_rcp_iflag_f32_e32 v7, v7
	v_max_i32_e32 v10, v6, v10
	v_xor_b32_e32 v8, v6, v9
	v_ashrrev_i32_e32 v8, 31, v8
	v_mul_f32_e32 v7, 0x4f7ffffe, v7
	v_cvt_u32_f32_e32 v7, v7
	v_mul_lo_u32 v11, v11, v7
	v_mul_hi_u32 v11, v7, v11
	v_add_u32_e32 v7, v7, v11
	v_mul_hi_u32 v7, v10, v7
	v_mul_lo_u32 v11, v7, v4
	v_sub_u32_e32 v10, v10, v11
	v_add_u32_e32 v12, 1, v7
	v_cmp_ge_u32_e32 vcc, v10, v4
	v_sub_u32_e32 v11, v10, v4
	s_nop 0
	v_cndmask_b32_e32 v7, v7, v12, vcc
	v_cndmask_b32_e32 v10, v10, v11, vcc
	v_add_u32_e32 v11, 1, v7
	v_cmp_ge_u32_e32 vcc, v10, v4
	s_nop 1
	v_cndmask_b32_e32 v4, v7, v11, vcc
	v_xor_b32_e32 v4, v4, v8
	v_sub_u32_e32 v4, v4, v8
	v_mul_lo_u32 v7, v4, v9
	v_sub_u32_e32 v6, v6, v7
	s_waitcnt lgkmcnt(0)
	v_lshl_add_u32 v3, v6, 8, v3

; #define GAS __attribute__((address_space(1)))
; #define LAS __attribute__((address_space(3)))
; __device__ __forceinline__ const float* modp(const unsigned char* ws, int layer, int r, int chunk) { return (const float*)(ws + WS_MOD) + ((size_t)(layer * 3 + r) * 6 + chunk) * D; }
; __device__ __forceinline__ void phase_combine(const Frame& F, const Args& a, int layer) {
;     bf16_t* X = (bf16_t*)(F.ws + WS_X); bf16_t* A0 = (bf16_t*)(F.ws + WS_A0); const unsigned char* YS = F.ws + WS_YS;
;     const int* TOK_SLOT = (const int*)(F.ws + WS_TOKSLOT); const float* SW = (const float*)(F.ws + WS_SELW); const int* EXPT = (const int*)(F.ws + WS_EXPT);
;     const int tok0 = layer ? TC : 0, TPB = layer ? 32 : 34; const int start64 = EXPT[64];
;     LAS float* P = (LAS float*)F.lds;
;     for (int i = F.tid; i < 11 * (D / 4); i += NTHREADS) { const int t = i / (D / 4), c = 4 * (i % (D / 4)); f32x4 v;
;         if (t == 0) v = *(const GAS f32x4*)(a.in[I_LNFG] + layer * D + c);
;         else if (t == 1) v = *(const GAS f32x4*)(a.in[I_LNFB] + layer * D + c);
;         else { const int r = (t - 2) / 3, k = (t - 2) % 3;
;             if (k == 0) v = *(const GAS f32x4*)(modp(F.ws, layer, r, 5) + c);
;             else if (layer == 0) { v = *(const GAS f32x4*)(modp(F.ws, 1, r, k == 1 ? 1 : 0) + c); if (k == 1) v = v + 1.0f; }
;             else v = (f32x4){0.f, 0.f, 0.f, 0.f}; }
;         *(LAS f32x4*)(P + t * D + c) = v; }
;     __syncthreads();
.LBB0_2368:
	s_cmp_lt_i32 s94, 12
	s_cselect_b64 s[0:1], -1, 0
	s_and_b64 s[0:1], s[0:1], s[4:5]
	s_andn2_b64 vcc, exec, s[0:1]
	v_lshl_add_u32 v202, v0, 4, 0
	s_cbranch_vccnz .LBB0_2393
	v_mov_b32_e32 v2, 0x420000
	global_load_dword v112, v2, s[92:93] offset:256
	s_add_u32 s4, s92, 0x100000
	s_addc_u32 s5, s93, 0
	v_mov_b32_e32 v7, 0
	v_lshlrev_b32_e32 v8, 2, v0
	s_mov_b64 s[6:7], 0
	v_mov_b32_e32 v9, -2
	s_movk_i32 s2, 0x1ff
	s_movk_i32 s16, 0x2000
	s_mov_b32 s17, 0x55555556
	s_movk_i32 s18, 0x13ff
	v_mov_b32_e32 v10, 0
	v_mov_b32_e32 v11, v0
	v_and_b32_e32 v12, 0x7fc, v8
	v_lshlrev_b32_e32 v6, 2, v12
	v_readlane_b32 s36, v254, 5
	v_readlane_b32 s37, v254, 6
	v_readlane_b32 s38, v254, 7
	v_readlane_b32 s39, v254, 8
	s_nop 4
	global_load_dwordx4 v[20:23], v6, s[36:37]
	global_load_dwordx4 v[24:27], v6, s[38:39]
	s_add_u32 s10, s4, 0xa000
	s_addc_u32 s11, s5, 0
	global_load_dwordx4 v[28:31], v6, s[10:11]
	s_add_u32 s10, s4, 0x26000
	s_addc_u32 s11, s5, 0
	global_load_dwordx4 v[32:35], v6, s[10:11]
	s_add_u32 s10, s4, 0x24000
	s_addc_u32 s11, s5, 0
	global_load_dwordx4 v[36:39], v6, s[10:11]
	s_add_u32 s10, s4, 0x16000
	s_addc_u32 s11, s5, 0
	global_load_dwordx4 v[40:43], v6, s[10:11]
	s_add_u32 s10, s4, 0x32000
	s_addc_u32 s11, s5, 0
	global_load_dwordx4 v[44:47], v6, s[10:11]
	s_add_u32 s10, s4, 0x30000
	s_addc_u32 s11, s5, 0
	global_load_dwordx4 v[48:51], v6, s[10:11]
	s_add_u32 s10, s4, 0x22000
	s_addc_u32 s11, s5, 0
	global_load_dwordx4 v[52:55], v6, s[10:11]
	s_add_u32 s10, s4, 0x3e000
	s_addc_u32 s11, s5, 0
	global_load_dwordx4 v[56:59], v6, s[10:11]
	s_add_u32 s10, s4, 0x3c000
	s_addc_u32 s11, s5, 0
	global_load_dwordx4 v[60:63], v6, s[10:11]
	s_waitcnt vmcnt(0)
	v_pk_add_f32 v[32:33], v[32:33], 1.0 op_sel_hi:[1,0]
	v_pk_add_f32 v[34:35], v[34:35], 1.0 op_sel_hi:[1,0]
	v_pk_add_f32 v[44:45], v[44:45], 1.0 op_sel_hi:[1,0]
	v_pk_add_f32 v[46:47], v[46:47], 1.0 op_sel_hi:[1,0]
	v_pk_add_f32 v[56:57], v[56:57], 1.0 op_sel_hi:[1,0]
	v_pk_add_f32 v[58:59], v[58:59], 1.0 op_sel_hi:[1,0]
	v_add_u32_e32 v6, 0x10000, v202
	ds_write_b128 v202, v[20:23]
	ds_write_b128 v202, v[24:27] offset:8192
	ds_write_b128 v202, v[28:31] offset:16384
	ds_write_b128 v202, v[32:35] offset:24576
	ds_write_b128 v202, v[36:39] offset:32768
	ds_write_b128 v202, v[40:43] offset:40960
	ds_write_b128 v202, v[44:47] offset:49152
	ds_write_b128 v202, v[48:51] offset:57344
	ds_write_b128 v6, v[52:55]
	ds_write_b128 v6, v[56:59] offset:8192
	ds_write_b128 v6, v[60:63] offset:16384

; #define GAS __attribute__((address_space(1)))
; #define LAS __attribute__((address_space(3)))
; __device__ __forceinline__ const float* modp(const unsigned char* ws, int layer, int r, int chunk) { return (const float*)(ws + WS_MOD) + ((size_t)(layer * 3 + r) * 6 + chunk) * D; }
; __device__ __forceinline__ void phase_combine(const Frame& F, const Args& a, int layer) {
;     bf16_t* X = (bf16_t*)(F.ws + WS_X); bf16_t* A0 = (bf16_t*)(F.ws + WS_A0); const unsigned char* YS = F.ws + WS_YS;
;     const int* TOK_SLOT = (const int*)(F.ws + WS_TOKSLOT); const float* SW = (const float*)(F.ws + WS_SELW); const int* EXPT = (const int*)(F.ws + WS_EXPT);
;     const int tok0 = layer ? TC : 0, TPB = layer ? 32 : 34; const int start64 = EXPT[64];
;     LAS float* P = (LAS float*)F.lds;
;     for (int i = F.tid; i < 11 * (D / 4); i += NTHREADS) { const int t = i / (D / 4), c = 4 * (i % (D / 4)); f32x4 v;
;         if (t == 0) v = *(const GAS f32x4*)(a.in[I_LNFG] + layer * D + c);
;         else if (t == 1) v = *(const GAS f32x4*)(a.in[I_LNFB] + layer * D + c);
;         else { const int r = (t - 2) / 3, k = (t - 2) % 3;
;             if (k == 0) v = *(const GAS f32x4*)(modp(F.ws, layer, r, 5) + c);
;             else if (layer == 0) { v = *(const GAS f32x4*)(modp(F.ws, 1, r, k == 1 ? 1 : 0) + c); if (k == 1) v = v + 1.0f; }
;             else v = (f32x4){0.f, 0.f, 0.f, 0.f}; }
;         *(LAS f32x4*)(P + t * D + c) = v; }
;     __syncthreads();
.LBB0_3515:
	s_cmp_lt_i32 s94, 20
	s_cselect_b64 s[0:1], -1, 0
	s_and_b64 s[0:1], s[0:1], s[4:5]
	s_andn2_b64 vcc, exec, s[0:1]
	s_cbranch_vccnz .LBB0_3534
	v_mov_b32_e32 v2, 0x420000
	global_load_dword v2, v2, s[92:93] offset:256
	v_readlane_b32 s36, v254, 5
	v_readlane_b32 s37, v254, 6
	s_add_u32 s0, s92, 0x100000
	v_readlane_b32 s38, v254, 7
	v_readlane_b32 s39, v254, 8
	s_mov_b64 s[8:9], s[36:37]
	s_addc_u32 s1, s93, 0
	s_mov_b64 s[10:11], s[38:39]
	s_add_u32 s6, s10, 0x2000
	s_addc_u32 s7, s11, 0
	s_add_u32 s8, s8, 0x2000
	v_mov_b32_e32 v7, 0
	s_mov_b64 s[4:5], 0
	v_mov_b32_e32 v10, -2
	s_movk_i32 s2, 0x200
	s_movk_i32 s21, 0x1ff
	s_movk_i32 s22, 0x2000
	s_mov_b32 s23, 0x55555556
	s_movk_i32 s24, 0x13ff
	s_addc_u32 s9, s9, 0
	v_mov_b32_e32 v11, 0
	v_readlane_b32 s40, v254, 9
	v_readlane_b32 s41, v254, 10
	v_readlane_b32 s42, v254, 11
	v_readlane_b32 s43, v254, 12
	v_readlane_b32 s44, v254, 13
	v_readlane_b32 s45, v254, 14
	v_readlane_b32 s46, v254, 15
	v_readlane_b32 s47, v254, 16
	v_readlane_b32 s48, v254, 17
	v_readlane_b32 s49, v254, 18
	v_readlane_b32 s50, v254, 19
	v_readlane_b32 s51, v254, 20
	s_waitcnt vmcnt(0)
	v_readfirstlane_b32 s20, v2
	v_and_b32_e32 v2, 0x7fc, v248
	v_lshlrev_b32_e32 v6, 2, v2
	global_load_dwordx4 v[20:23], v6, s[8:9]
	global_load_dwordx4 v[24:27], v6, s[6:7]
	s_add_u32 s10, s0, 0x2e000
	s_addc_u32 s11, s1, 0
	global_load_dwordx4 v[28:31], v6, s[10:11]
	s_add_u32 s10, s0, 0x3a000
	s_addc_u32 s11, s1, 0
	global_load_dwordx4 v[32:35], v6, s[10:11]
	s_add_u32 s10, s0, 0x46000
	s_addc_u32 s11, s1, 0
	global_load_dwordx4 v[36:39], v6, s[10:11]
	v_mov_b32_e32 v40, 0
	v_mov_b32_e32 v41, 0
	v_mov_b32_e32 v42, 0
	v_mov_b32_e32 v43, 0
	v_add_u32_e32 v6, 0x10000, v202
	s_waitcnt vmcnt(0)
	ds_write_b128 v202, v[20:23]
	ds_write_b128 v202, v[24:27] offset:8192
	ds_write_b128 v202, v[28:31] offset:16384
	ds_write_b128 v202, v[40:43] offset:24576
	ds_write_b128 v202, v[40:43] offset:32768
	ds_write_b128 v202, v[32:35] offset:40960
	ds_write_b128 v202, v[40:43] offset:49152
	ds_write_b128 v202, v[40:43] offset:57344
	ds_write_b128 v6, v[36:39]
	ds_write_b128 v6, v[40:43] offset:8192
	ds_write_b128 v6, v[40:43] offset:16384
